# dense attention loop head aligned to 64 bytes
# baseline (speedup 1.0000x reference)
.LBB0_408:
	s_lshr_b32 s4, s72, 3
	s_lshl_b32 s5, s72, 5
	s_bfe_u32 s10, s72, 0x20001
	s_ashr_i32 s9, s72, 8
	s_and_b32 s4, s4, 16
	s_and_b32 s11, s5, 32
	s_lshl_b32 s8, s10, 7
	s_or_b32 s4, s11, s4
	s_lshl_b32 s13, s9, 12
	s_mul_i32 s11, s9, 0x5c00000
	s_mul_hi_i32 s12, s13, 0x5c00
	s_add_u32 s11, s18, s11
	s_addc_u32 s12, s19, s12
	s_and_b32 s14, s5, 0xf00
	s_mul_i32 s5, s14, 0x5c00
	s_add_u32 s5, s11, s5
	s_addc_u32 s11, s12, 0
	s_lshl_b32 s12, s10, 9
	s_lshl_b32 s4, s4, 3
	s_or_b32 s12, s4, s12
	s_lshl_b32 s4, s12, 1
	s_add_u32 s4, s5, s4
	s_addc_u32 s5, s11, 0
	v_mov_b32_e32 v147, v3
	v_lshl_add_u64 v[8:9], s[4:5], 0, v[146:147]
	v_add_co_u32_e32 v4, vcc, s54, v8
	v_lshl_add_u64 v[32:33], v[8:9], 0, s[24:25]
	s_nop 0
	v_addc_co_u32_e32 v5, vcc, 0, v9, vcc
	global_load_dwordx4 v[4:7], v[4:5], off offset:1024
	s_nop 0
	global_load_dwordx4 v[8:11], v[32:33], off offset:16
	global_load_dwordx4 v[12:15], v[32:33], off offset:32
	global_load_dwordx4 v[16:19], v[32:33], off offset:48
	global_load_dwordx4 v[20:23], v[32:33], off offset:128
	global_load_dwordx4 v[24:27], v[32:33], off offset:160
	global_load_dwordx4 v[28:31], v[32:33], off offset:144
	s_lshl_b32 s4, s9, 2
	s_or_b32 s10, s4, s10
	s_lshl_b32 s4, s10, 12
	s_ashr_i32 s5, s4, 31
	global_load_dwordx4 v[32:35], v[32:33], off offset:176
	s_lshl_b64 s[4:5], s[4:5], 7
	s_add_u32 s4, s49, s4
	s_addc_u32 s5, s50, s5
	s_lshl_b32 s10, s10, 7
	s_ashr_i32 s11, s10, 31
	v_lshl_add_u64 v[36:37], s[4:5], 0, v[138:139]
	s_lshl_b64 s[10:11], s[10:11], 12
	v_lshl_add_u64 v[38:39], v[36:37], 0, v[136:137]
	v_lshl_add_u64 v[36:37], v[140:141], 0, s[10:11]
	global_load_dwordx4 v[40:43], v[36:37], off
	global_load_dwordx4 v[44:47], v[38:39], off
	v_mov_b32_e32 v106, v3
	v_mov_b32_e32 v100, v3
	v_mov_b32_e32 v101, v3
	v_mov_b32_e32 v107, v3
	v_mov_b32_e32 v108, v3
	v_mov_b32_e32 v109, v3
	v_mov_b32_e32 v110, v3
	v_mov_b32_e32 v111, v3
	v_mov_b32_e32 v112, v3
	v_mov_b32_e32 v113, v3
	v_mov_b32_e32 v114, v3
	v_mov_b32_e32 v102, v3
	v_mov_b32_e32 v103, v3
	v_mov_b32_e32 v104, v3
	v_mov_b32_e32 v105, v3
	s_waitcnt vmcnt(0)
	v_mov_b32_e32 v115, v3
	v_lshl_add_u64 v[148:149], s[4:5], 0, v[136:137]
	s_mov_b32 s15, 1
	v_mov_b32_e32 v145, 0
	v_mov_b32_e32 v152, v186
	s_waitcnt vmcnt(8)
	v_lshlrev_b32_e32 v51, 16, v8
	v_and_b32_e32 v8, 0xffff0000, v8
	s_waitcnt vmcnt(6)
	v_lshlrev_b32_e32 v59, 16, v16
	v_and_b32_e32 v16, 0xffff0000, v16
	v_lshlrev_b32_e32 v2, 16, v4
	v_and_b32_e32 v4, 0xffff0000, v4
	v_mul_f32_e32 v59, 0x3f8293ee, v59
	v_mul_f32_e32 v16, 0x3f8293ee, v16
	v_cvt_pk_fp8_f32 v106, v59, v16
	v_mul_f32_e32 v2, 0x3f8293ee, v2
	v_mul_f32_e32 v4, 0x3f8293ee, v4
	v_cvt_pk_fp8_f32 v100, v2, v4
	v_lshlrev_b32_e32 v60, 16, v17
	v_and_b32_e32 v2, 0xffff0000, v17
	v_lshlrev_b32_e32 v48, 16, v5
	v_and_b32_e32 v5, 0xffff0000, v5
	v_lshlrev_b32_e32 v49, 16, v6
	v_and_b32_e32 v6, 0xffff0000, v6
	v_mul_f32_e32 v60, 0x3f8293ee, v60
	v_mul_f32_e32 v2, 0x3f8293ee, v2
	v_cvt_pk_fp8_f32 v106, v60, v2 op_sel:[0,0,1]
	v_lshlrev_b32_e32 v2, 16, v18
	v_and_b32_e32 v4, 0xffff0000, v18
	v_mul_f32_e32 v49, 0x3f8293ee, v49
	v_mul_f32_e32 v6, 0x3f8293ee, v6
	v_cvt_pk_fp8_f32 v101, v49, v6
	v_mul_f32_e32 v48, 0x3f8293ee, v48
	v_mul_f32_e32 v5, 0x3f8293ee, v5
	v_cvt_pk_fp8_f32 v100, v48, v5 op_sel:[0,0,1]
	v_mul_f32_e32 v2, 0x3f8293ee, v2
	v_mul_f32_e32 v4, 0x3f8293ee, v4
	v_cvt_pk_fp8_f32 v107, v2, v4
	s_waitcnt vmcnt(5)
	v_lshlrev_b32_e32 v5, 16, v20
	v_and_b32_e32 v6, 0xffff0000, v20
	v_mul_f32_e32 v5, 0x3f8293ee, v5
	v_mul_f32_e32 v6, 0x3f8293ee, v6
	v_cvt_pk_fp8_f32 v108, v5, v6
	v_lshlrev_b32_e32 v2, 16, v19
	v_and_b32_e32 v4, 0xffff0000, v19
	v_mul_f32_e32 v2, 0x3f8293ee, v2
	v_mul_f32_e32 v4, 0x3f8293ee, v4
	v_cvt_pk_fp8_f32 v107, v2, v4 op_sel:[0,0,1]
	v_lshlrev_b32_e32 v2, 16, v21
	v_and_b32_e32 v4, 0xffff0000, v21
	v_mul_f32_e32 v2, 0x3f8293ee, v2
	v_mul_f32_e32 v4, 0x3f8293ee, v4
	v_cvt_pk_fp8_f32 v108, v2, v4 op_sel:[0,0,1]
	v_lshlrev_b32_e32 v2, 16, v22
	v_and_b32_e32 v4, 0xffff0000, v22
	v_mul_f32_e32 v2, 0x3f8293ee, v2
	v_mul_f32_e32 v4, 0x3f8293ee, v4
	v_cvt_pk_fp8_f32 v109, v2, v4
	s_waitcnt vmcnt(3)
	v_lshlrev_b32_e32 v5, 16, v28
	v_and_b32_e32 v6, 0xffff0000, v28
	v_mul_f32_e32 v5, 0x3f8293ee, v5
	v_mul_f32_e32 v6, 0x3f8293ee, v6
	v_cvt_pk_fp8_f32 v110, v5, v6
	v_lshlrev_b32_e32 v2, 16, v23
	v_and_b32_e32 v4, 0xffff0000, v23
	v_mul_f32_e32 v2, 0x3f8293ee, v2
	v_mul_f32_e32 v4, 0x3f8293ee, v4
	v_cvt_pk_fp8_f32 v109, v2, v4 op_sel:[0,0,1]
	v_lshlrev_b32_e32 v2, 16, v29
	v_and_b32_e32 v4, 0xffff0000, v29
	v_mul_f32_e32 v2, 0x3f8293ee, v2
	v_mul_f32_e32 v4, 0x3f8293ee, v4
	v_cvt_pk_fp8_f32 v110, v2, v4 op_sel:[0,0,1]
	v_lshlrev_b32_e32 v2, 16, v30
	v_and_b32_e32 v4, 0xffff0000, v30
	v_mul_f32_e32 v2, 0x3f8293ee, v2
	v_mul_f32_e32 v4, 0x3f8293ee, v4
	v_cvt_pk_fp8_f32 v111, v2, v4
	v_lshlrev_b32_e32 v5, 16, v24
	v_and_b32_e32 v6, 0xffff0000, v24
	v_mul_f32_e32 v5, 0x3f8293ee, v5
	v_mul_f32_e32 v6, 0x3f8293ee, v6
	v_cvt_pk_fp8_f32 v112, v5, v6
	v_lshlrev_b32_e32 v2, 16, v31
	v_and_b32_e32 v4, 0xffff0000, v31
	v_mul_f32_e32 v2, 0x3f8293ee, v2
	v_mul_f32_e32 v4, 0x3f8293ee, v4
	v_cvt_pk_fp8_f32 v111, v2, v4 op_sel:[0,0,1]
	v_lshlrev_b32_e32 v2, 16, v25
	v_and_b32_e32 v4, 0xffff0000, v25
	v_mul_f32_e32 v2, 0x3f8293ee, v2
	v_mul_f32_e32 v4, 0x3f8293ee, v4
	v_cvt_pk_fp8_f32 v112, v2, v4 op_sel:[0,0,1]
	v_lshlrev_b32_e32 v2, 16, v26
	v_and_b32_e32 v4, 0xffff0000, v26
	v_mul_f32_e32 v2, 0x3f8293ee, v2
	v_mul_f32_e32 v4, 0x3f8293ee, v4
	v_cvt_pk_fp8_f32 v113, v2, v4
	s_waitcnt vmcnt(2)
	v_lshlrev_b32_e32 v5, 16, v32
	v_and_b32_e32 v6, 0xffff0000, v32
	v_lshlrev_b32_e32 v53, 16, v10
	v_and_b32_e32 v10, 0xffff0000, v10
	v_mul_f32_e32 v5, 0x3f8293ee, v5
	v_mul_f32_e32 v6, 0x3f8293ee, v6
	v_cvt_pk_fp8_f32 v114, v5, v6
	v_mul_f32_e32 v51, 0x3f8293ee, v51
	v_mul_f32_e32 v8, 0x3f8293ee, v8
	v_cvt_pk_fp8_f32 v102, v51, v8
	v_mul_f32_e32 v53, 0x3f8293ee, v53
	v_mul_f32_e32 v10, 0x3f8293ee, v10
	v_cvt_pk_fp8_f32 v103, v53, v10
	v_lshlrev_b32_e32 v2, 16, v27
	v_and_b32_e32 v4, 0xffff0000, v27
	v_mul_f32_e32 v2, 0x3f8293ee, v2
	v_mul_f32_e32 v4, 0x3f8293ee, v4
	v_cvt_pk_fp8_f32 v113, v2, v4 op_sel:[0,0,1]
	v_lshlrev_b32_e32 v2, 16, v33
	v_and_b32_e32 v4, 0xffff0000, v33
	v_lshlrev_b32_e32 v50, 16, v7
	v_and_b32_e32 v7, 0xffff0000, v7
	v_lshlrev_b32_e32 v52, 16, v9
	v_and_b32_e32 v9, 0xffff0000, v9
	v_lshlrev_b32_e32 v54, 16, v11
	v_and_b32_e32 v11, 0xffff0000, v11
	v_mul_f32_e32 v2, 0x3f8293ee, v2
	v_mul_f32_e32 v4, 0x3f8293ee, v4
	v_cvt_pk_fp8_f32 v114, v2, v4 op_sel:[0,0,1]
	s_waitcnt vmcnt(1)
	v_mov_b32_e32 v4, v40
	v_mov_b32_e32 v5, v42
	v_mov_b32_e32 v42, v41
	v_lshlrev_b32_e32 v55, 16, v12
	v_and_b32_e32 v12, 0xffff0000, v12
	v_lshlrev_b32_e32 v57, 16, v14
	v_and_b32_e32 v14, 0xffff0000, v14
	v_mul_f32_e32 v50, 0x3f8293ee, v50
	v_mul_f32_e32 v7, 0x3f8293ee, v7
	v_cvt_pk_fp8_f32 v101, v50, v7 op_sel:[0,0,1]
	v_mul_f32_e32 v52, 0x3f8293ee, v52
	v_mul_f32_e32 v9, 0x3f8293ee, v9
	v_cvt_pk_fp8_f32 v102, v52, v9 op_sel:[0,0,1]
	v_mul_f32_e32 v54, 0x3f8293ee, v54
	v_mul_f32_e32 v11, 0x3f8293ee, v11
	v_cvt_pk_fp8_f32 v103, v54, v11 op_sel:[0,0,1]
	ds_write_b64 v189, v[4:5]
	ds_write_b64 v190, v[42:43]
	s_waitcnt vmcnt(0)
	ds_write_b128 v191, v[44:47] offset:32768
	s_waitcnt lgkmcnt(0)
	s_barrier
	ds_read_b128 v[40:43], v192 offset:36864
	ds_read_b128 v[4:7], v192 offset:32768
	ds_read_b128 v[44:47], v193 offset:36864
	ds_read_b128 v[8:11], v193 offset:32768
	v_mul_f32_e32 v55, 0x3f8293ee, v55
	v_mul_f32_e32 v12, 0x3f8293ee, v12
	v_cvt_pk_fp8_f32 v104, v55, v12
	v_mul_f32_e32 v57, 0x3f8293ee, v57
	v_mul_f32_e32 v14, 0x3f8293ee, v14
	v_cvt_pk_fp8_f32 v105, v57, v14
	v_lshlrev_b32_e32 v56, 16, v13
	v_and_b32_e32 v13, 0xffff0000, v13
	v_lshlrev_b32_e32 v58, 16, v15
	v_and_b32_e32 v15, 0xffff0000, v15
	v_lshlrev_b32_e32 v2, 16, v34
	v_and_b32_e32 v12, 0xffff0000, v34
	v_mul_f32_e32 v56, 0x3f8293ee, v56
	v_mul_f32_e32 v13, 0x3f8293ee, v13
	v_cvt_pk_fp8_f32 v104, v56, v13 op_sel:[0,0,1]
	v_mul_f32_e32 v58, 0x3f8293ee, v58
	v_mul_f32_e32 v15, 0x3f8293ee, v15
	v_cvt_pk_fp8_f32 v105, v58, v15 op_sel:[0,0,1]
	v_mul_f32_e32 v2, 0x3f8293ee, v2
	v_mul_f32_e32 v12, 0x3f8293ee, v12
	v_cvt_pk_fp8_f32 v115, v2, v12
	v_lshlrev_b32_e32 v2, 16, v35
	v_and_b32_e32 v56, 0xffff0000, v35
	s_waitcnt lgkmcnt(0)
	v_mfma_scale_f32_32x32x64_f8f6f4 v[20:35], v[4:11], v[100:107], 0, v188, v188 op_sel_hi:[0,0,0]
	v_mfma_scale_f32_32x32x64_f8f6f4 v[4:19], v[40:47], v[100:107], 0, v188, v188 op_sel_hi:[0,0,0]
	ds_read_b128 v[40:43], v194 offset:36864
	ds_read_b128 v[48:51], v194 offset:32768
	ds_read_b128 v[44:47], v195 offset:36864
	ds_read_b128 v[52:55], v195 offset:32768
	v_mul_f32_e32 v2, 0x3f8293ee, v2
	v_mul_f32_e32 v56, 0x3f8293ee, v56
	v_cvt_pk_fp8_f32 v115, v2, v56 op_sel:[0,0,1]
	s_waitcnt lgkmcnt(0)
	v_mfma_scale_f32_32x32x64_f8f6f4 v[20:35], v[48:55], v[108:115], v[20:35], v188, v188 op_sel_hi:[0,0,0]
	v_mfma_scale_f32_32x32x64_f8f6f4 v[4:19], v[40:47], v[108:115], v[4:19], v188, v188 op_sel_hi:[0,0,0]
	v_add_co_u32_e32 v44, vcc, s56, v38
	s_nop 15
	s_nop 15
	s_nop 0
	v_max_f32_e32 v2, v21, v21
	v_max_f32_e32 v40, v20, v20
	v_max_f32_e32 v2, v40, v2
	v_max3_f32 v2, v2, v22, v23
	v_max3_f32 v2, v2, v24, v25
	v_max3_f32 v2, v2, v26, v27
	v_max3_f32 v2, v2, v28, v29
	v_max3_f32 v2, v2, v30, v31
	v_max3_f32 v2, v2, v32, v33
	v_max3_f32 v2, v2, v34, v35
	v_max3_f32 v2, v2, v4, v5
	v_max3_f32 v2, v2, v6, v7
	v_max3_f32 v2, v2, v8, v9
	v_max3_f32 v2, v2, v10, v11
	v_max3_f32 v2, v2, v12, v13
	v_max3_f32 v2, v2, v14, v15
	v_max3_f32 v2, v2, v16, v17
	v_max3_f32 v2, v2, v18, v19
	v_mov_b32_e32 v48, v2
	s_nop 1
	v_permlane32_swap_b32_e32 v2, v48
	v_max_f32_e32 v48, v48, v48
	v_max_f32_e32 v2, v2, v2
	v_max_f32_e32 v2, v2, v48
	v_addc_co_u32_e32 v45, vcc, 0, v39, vcc
	v_add_f32_e32 v48, 0x7149f2ca, v2
	v_max_f32_e32 v2, 0xf149f2ca, v2
	v_cmp_ge_f32_e32 vcc, s55, v48
	v_sub_f32_e32 v48, 0xf149f2ca, v2
	v_mul_f32_e32 v48, 0x3e000000, v48
	v_exp_f32_e32 v48, v48
	global_load_dwordx4 v[40:43], v[36:37], off offset:64
	s_cmp_eq_u64 vcc, exec
	s_cselect_b64 vcc, -1, 0
	global_load_dwordx4 v[44:47], v[44:45], off
	v_cndmask_b32_e32 v153, v2, v196, vcc
	v_cndmask_b32_e64 v147, v48, 1.0, vcc
	v_add_co_u32_e32 v38, vcc, s52, v38
	v_mul_f32_e32 v2, 0xbe000000, v153
	s_nop 0
	v_addc_co_u32_e32 v39, vcc, 0, v39, vcc
	global_load_dwordx4 v[120:123], v[38:39], off
	global_load_dwordx4 v[116:119], v[36:37], off offset:128
	v_mov_b32_e32 v36, v2
	v_fmamk_f32 v20, v20, 0x3e000000, v2
	v_fmamk_f32 v21, v21, 0x3e000000, v2
	v_fmamk_f32 v22, v22, 0x3e000000, v2
	v_fmamk_f32 v23, v23, 0x3e000000, v2
	v_fmamk_f32 v24, v24, 0x3e000000, v2
	v_fmamk_f32 v25, v25, 0x3e000000, v2
	v_fmamk_f32 v26, v26, 0x3e000000, v2
	v_fmamk_f32 v27, v27, 0x3e000000, v2
	v_fmamk_f32 v28, v28, 0x3e000000, v2
	v_fmamk_f32 v29, v29, 0x3e000000, v2
	v_fmamk_f32 v30, v30, 0x3e000000, v2
	v_fmamk_f32 v31, v31, 0x3e000000, v2
	v_fmamk_f32 v32, v32, 0x3e000000, v2
	v_fmamk_f32 v33, v33, 0x3e000000, v2
	v_fmamk_f32 v34, v34, 0x3e000000, v2
	v_fmac_f32_e32 v36, 0x3e000000, v35
	s_lshl_b32 s4, s9, 9
	v_pk_fma_f32 v[158:159], v[16:17], s[26:27], v[2:3] op_sel_hi:[1,0,0]
	v_pk_fma_f32 v[154:155], v[4:5], s[26:27], v[2:3] op_sel_hi:[1,0,0]
	v_exp_f32_e32 v173, v20
	v_exp_f32_e32 v177, v21
	v_exp_f32_e32 v165, v22
	v_exp_f32_e32 v166, v23
	v_exp_f32_e32 v174, v24
	v_exp_f32_e32 v178, v25
	v_exp_f32_e32 v167, v26
	v_exp_f32_e32 v168, v27
	v_exp_f32_e32 v175, v28
	v_exp_f32_e32 v179, v29
	v_exp_f32_e32 v169, v30
	v_exp_f32_e32 v170, v31
	v_exp_f32_e32 v176, v32
	v_exp_f32_e32 v180, v33
	v_exp_f32_e32 v171, v34
	v_exp_f32_e32 v172, v36
	s_or_b32 s4, s4, s8
	v_mov_b32_e32 v16, v3
	v_mov_b32_e32 v17, v3
	v_pk_fma_f32 v[156:157], v[18:19], s[26:27], v[2:3] op_sel_hi:[1,0,0]
	v_pk_fma_f32 v[160:161], v[14:15], s[26:27], v[2:3] op_sel_hi:[1,0,0]
	v_pk_fma_f32 v[124:125], v[12:13], s[26:27], v[2:3] op_sel_hi:[1,0,0]
	v_pk_fma_f32 v[126:127], v[10:11], s[26:27], v[2:3] op_sel_hi:[1,0,0]
	v_pk_fma_f32 v[128:129], v[8:9], s[26:27], v[2:3] op_sel_hi:[1,0,0]
	v_pk_fma_f32 v[130:131], v[6:7], s[26:27], v[2:3] op_sel_hi:[1,0,0]
	s_waitcnt vmcnt(2)
	s_ashr_i32 s5, s4, 31
	v_mov_b32_e32 v2, v3
	v_mov_b32_e32 v6, v3
	v_mov_b32_e32 v7, v3
	v_mov_b32_e32 v8, v3
	v_mov_b32_e32 v9, v3
	v_mov_b32_e32 v10, v3
	v_mov_b32_e32 v11, v3
	v_mov_b32_e32 v12, v3
	v_mov_b32_e32 v13, v3
	v_mov_b32_e32 v14, v3
	v_mov_b32_e32 v15, v3
	s_lshl_b64 s[4:5], s[4:5], 12
	v_lshl_add_u64 v[150:151], v[142:143], 0, s[4:5]
	s_waitcnt vmcnt(3)
	v_mov_b32_e32 v4, v40
	v_mov_b32_e32 v5, v42
	v_mov_b32_e32 v42, v41
	ds_write_b64 v189, v[4:5] offset:16384
	ds_write_b64 v190, v[42:43] offset:16384
	s_waitcnt vmcnt(2)
	ds_write_b128 v191, v[44:47] offset:49152
	v_mov_b32_e32 v4, v3
	v_mov_b32_e32 v5, v3
	v_mov_b64_e32 v[66:67], v[16:17]
	v_mov_b64_e32 v[50:51], v[16:17]
	v_mov_b64_e32 v[34:35], v[16:17]
	v_mov_b64_e32 v[64:65], v[14:15]
	v_mov_b64_e32 v[62:63], v[12:13]
	v_mov_b64_e32 v[60:61], v[10:11]
	v_mov_b64_e32 v[58:59], v[8:9]
	v_mov_b64_e32 v[56:57], v[6:7]
	v_mov_b64_e32 v[54:55], v[4:5]
	v_mov_b64_e32 v[52:53], v[2:3]
	v_mov_b64_e32 v[48:49], v[14:15]
	v_mov_b64_e32 v[46:47], v[12:13]
	v_mov_b64_e32 v[44:45], v[10:11]
	v_mov_b64_e32 v[42:43], v[8:9]
	v_mov_b64_e32 v[40:41], v[6:7]
	v_mov_b64_e32 v[38:39], v[4:5]
	v_mov_b64_e32 v[36:37], v[2:3]
	v_mov_b64_e32 v[32:33], v[14:15]
	v_mov_b64_e32 v[30:31], v[12:13]
	v_mov_b64_e32 v[28:29], v[10:11]
	v_mov_b64_e32 v[26:27], v[8:9]
	v_mov_b64_e32 v[24:25], v[6:7]
	v_mov_b64_e32 v[22:23], v[4:5]
	v_mov_b64_e32 v[20:21], v[2:3]
	v_mov_b64_e32 v[18:19], v[16:17]
	v_mov_b64_e32 v[16:17], v[14:15]
	v_mov_b64_e32 v[14:15], v[12:13]
	v_mov_b64_e32 v[12:13], v[10:11]
	v_mov_b64_e32 v[10:11], v[8:9]
	v_mov_b64_e32 v[8:9], v[6:7]
	v_mov_b64_e32 v[6:7], v[4:5]
	v_mov_b64_e32 v[4:5], v[2:3]
	s_waitcnt lgkmcnt(0)
	s_barrier
	v_exp_f32_e32 v154, v154
	v_exp_f32_e32 v155, v155
	v_exp_f32_e32 v130, v130
	v_exp_f32_e32 v131, v131
	v_exp_f32_e32 v128, v128
	v_exp_f32_e32 v129, v129
	v_exp_f32_e32 v126, v126
	v_exp_f32_e32 v127, v127
	v_exp_f32_e32 v124, v124
	v_exp_f32_e32 v125, v125
	v_exp_f32_e32 v160, v160
	v_exp_f32_e32 v161, v161
	v_exp_f32_e32 v158, v158
	v_exp_f32_e32 v159, v159
	v_exp_f32_e32 v156, v156
	v_exp_f32_e32 v157, v157
	v_mul_f32_e32 v216, 0xbe000000, v153
	v_mov_b32_e32 v217, v216
	v_mov_b32_e32 v218, v216
	v_mov_b32_e32 v219, v216
	v_mov_b32_e32 v220, v216
	v_mov_b32_e32 v221, v216
	v_mov_b32_e32 v222, v216
	v_mov_b32_e32 v223, v216
	v_mov_b32_e32 v224, v216
	v_mov_b32_e32 v225, v216
	v_mov_b32_e32 v226, v216
	v_mov_b32_e32 v227, v216
	v_mov_b32_e32 v228, v216
	v_mov_b32_e32 v229, v216
	v_mov_b32_e32 v230, v216
	v_mov_b32_e32 v231, v216
	v_mov_b32_e32 v247, 0x7c7c7c7c
	.p2alignl 6, 3212836864
